# v11 + bias1 (pe x cmp_w1 column sums) spread over 64 WGs x 16 columns instead of 4 WGs, fixed-order LDS reduction
# baseline (speedup 1.0000x reference)
.LBB0_183:
	s_or_b64 exec, exec, s[6:7]
	s_cmp_lt_u32 s88, 64
	s_cbranch_scc0 .LBB0_187
	s_load_dwordx4 s[16:19], s[0:1], 0x60
	v_readfirstlane_b32 s6, v4
	v_and_b32_e32 v0, 63, v4
	v_lshrrev_b32_e32 v1, 2, v0
	v_and_b32_e32 v0, 3, v0
	v_lshlrev_b32_e32 v0, 4, v0
	v_lshl_add_u32 v0, v1, 10, v0
	v_lshlrev_b32_e32 v1, 2, v1
	v_mov_b32_e32 v8, 0
	v_mov_b32_e32 v9, 0
	v_mov_b32_e32 v10, 0
	v_mov_b32_e32 v11, 0
	s_lshr_b32 s3, s88, 4
	s_and_b32 s10, s88, 15
	s_lshl_b32 s7, s3, 13
	s_lshl_b32 s8, s6, 4
	s_add_u32 s7, s7, s8
	s_lshl_b32 s9, s3, 21
	s_lshl_b32 s8, s6, 12
	s_add_u32 s9, s9, s8
	s_lshl_b32 s8, s10, 6
	s_add_u32 s9, s9, s8
	s_waitcnt lgkmcnt(0)
	s_add_u32 s16, s16, s7
	s_addc_u32 s17, s17, 0
	s_add_u32 s18, s18, s9
	s_addc_u32 s19, s19, 0
	global_load_dword v16, v1, s[16:17]
	global_load_dword v17, v1, s[16:17] offset:64
	global_load_dword v18, v1, s[16:17] offset:128
	global_load_dword v19, v1, s[16:17] offset:192
	global_load_dword v20, v1, s[16:17] offset:256
	global_load_dword v21, v1, s[16:17] offset:320
	global_load_dword v22, v1, s[16:17] offset:384
	global_load_dword v23, v1, s[16:17] offset:448
	global_load_dword v24, v1, s[16:17] offset:512
	global_load_dword v25, v1, s[16:17] offset:576
	global_load_dword v26, v1, s[16:17] offset:640
	global_load_dword v27, v1, s[16:17] offset:704
	global_load_dword v28, v1, s[16:17] offset:768
	global_load_dword v29, v1, s[16:17] offset:832
	global_load_dword v30, v1, s[16:17] offset:896
	global_load_dword v31, v1, s[16:17] offset:960
	global_load_dwordx4 v[48:51], v0, s[18:19]
	s_add_u32 s18, s18, 0x4000
	s_addc_u32 s19, s19, 0
	global_load_dwordx4 v[52:55], v0, s[18:19]
	s_add_u32 s18, s18, 0x4000
	s_addc_u32 s19, s19, 0
	global_load_dwordx4 v[56:59], v0, s[18:19]
	s_add_u32 s18, s18, 0x4000
	s_addc_u32 s19, s19, 0
	global_load_dwordx4 v[60:63], v0, s[18:19]
	s_add_u32 s18, s18, 0x4000
	s_addc_u32 s19, s19, 0
	global_load_dwordx4 v[64:67], v0, s[18:19]
	s_add_u32 s18, s18, 0x4000
	s_addc_u32 s19, s19, 0
	global_load_dwordx4 v[68:71], v0, s[18:19]
	s_add_u32 s18, s18, 0x4000
	s_addc_u32 s19, s19, 0
	global_load_dwordx4 v[72:75], v0, s[18:19]
	s_add_u32 s18, s18, 0x4000
	s_addc_u32 s19, s19, 0
	global_load_dwordx4 v[76:79], v0, s[18:19]
	s_add_u32 s18, s18, 0x4000
	s_addc_u32 s19, s19, 0
	global_load_dwordx4 v[80:83], v0, s[18:19]
	s_add_u32 s18, s18, 0x4000
	s_addc_u32 s19, s19, 0
	global_load_dwordx4 v[84:87], v0, s[18:19]
	s_add_u32 s18, s18, 0x4000
	s_addc_u32 s19, s19, 0
	global_load_dwordx4 v[88:91], v0, s[18:19]
	s_add_u32 s18, s18, 0x4000
	s_addc_u32 s19, s19, 0
	global_load_dwordx4 v[92:95], v0, s[18:19]
	s_add_u32 s18, s18, 0x4000
	s_addc_u32 s19, s19, 0
	global_load_dwordx4 v[96:99], v0, s[18:19]
	s_add_u32 s18, s18, 0x4000
	s_addc_u32 s19, s19, 0
	global_load_dwordx4 v[100:103], v0, s[18:19]
	s_add_u32 s18, s18, 0x4000
	s_addc_u32 s19, s19, 0
	global_load_dwordx4 v[104:107], v0, s[18:19]
	s_add_u32 s18, s18, 0x4000
	s_addc_u32 s19, s19, 0
	global_load_dwordx4 v[108:111], v0, s[18:19]
	s_waitcnt vmcnt(0)
	v_fmac_f32_e32 v8, v16, v48
	v_fmac_f32_e32 v9, v16, v49
	v_fmac_f32_e32 v10, v16, v50
	v_fmac_f32_e32 v11, v16, v51
	v_fmac_f32_e32 v8, v17, v52
	v_fmac_f32_e32 v9, v17, v53
	v_fmac_f32_e32 v10, v17, v54
	v_fmac_f32_e32 v11, v17, v55
	v_fmac_f32_e32 v8, v18, v56
	v_fmac_f32_e32 v9, v18, v57
	v_fmac_f32_e32 v10, v18, v58
	v_fmac_f32_e32 v11, v18, v59
	v_fmac_f32_e32 v8, v19, v60
	v_fmac_f32_e32 v9, v19, v61
	v_fmac_f32_e32 v10, v19, v62
	v_fmac_f32_e32 v11, v19, v63
	v_fmac_f32_e32 v8, v20, v64
	v_fmac_f32_e32 v9, v20, v65
	v_fmac_f32_e32 v10, v20, v66
	v_fmac_f32_e32 v11, v20, v67
	v_fmac_f32_e32 v8, v21, v68
	v_fmac_f32_e32 v9, v21, v69
	v_fmac_f32_e32 v10, v21, v70
	v_fmac_f32_e32 v11, v21, v71
	v_fmac_f32_e32 v8, v22, v72
	v_fmac_f32_e32 v9, v22, v73
	v_fmac_f32_e32 v10, v22, v74
	v_fmac_f32_e32 v11, v22, v75
	v_fmac_f32_e32 v8, v23, v76
	v_fmac_f32_e32 v9, v23, v77
	v_fmac_f32_e32 v10, v23, v78
	v_fmac_f32_e32 v11, v23, v79
	v_fmac_f32_e32 v8, v24, v80
	v_fmac_f32_e32 v9, v24, v81
	v_fmac_f32_e32 v10, v24, v82
	v_fmac_f32_e32 v11, v24, v83
	v_fmac_f32_e32 v8, v25, v84
	v_fmac_f32_e32 v9, v25, v85
	v_fmac_f32_e32 v10, v25, v86
	v_fmac_f32_e32 v11, v25, v87
	v_fmac_f32_e32 v8, v26, v88
	v_fmac_f32_e32 v9, v26, v89
	v_fmac_f32_e32 v10, v26, v90
	v_fmac_f32_e32 v11, v26, v91
	v_fmac_f32_e32 v8, v27, v92
	v_fmac_f32_e32 v9, v27, v93
	v_fmac_f32_e32 v10, v27, v94
	v_fmac_f32_e32 v11, v27, v95
	v_fmac_f32_e32 v8, v28, v96
	v_fmac_f32_e32 v9, v28, v97
	v_fmac_f32_e32 v10, v28, v98
	v_fmac_f32_e32 v11, v28, v99
	v_fmac_f32_e32 v8, v29, v100
	v_fmac_f32_e32 v9, v29, v101
	v_fmac_f32_e32 v10, v29, v102
	v_fmac_f32_e32 v11, v29, v103
	v_fmac_f32_e32 v8, v30, v104
	v_fmac_f32_e32 v9, v30, v105
	v_fmac_f32_e32 v10, v30, v106
	v_fmac_f32_e32 v11, v30, v107
	v_fmac_f32_e32 v8, v31, v108
	v_fmac_f32_e32 v9, v31, v109
	v_fmac_f32_e32 v10, v31, v110
	v_fmac_f32_e32 v11, v31, v111
	v_lshlrev_b32_e32 v2, 4, v4
	v_add_u32_e32 v2, 0x22100, v2
	ds_write_b128 v2, v[8:11]
	s_waitcnt lgkmcnt(0)
	s_barrier
	v_and_b32_e32 v2, 15, v4
	v_lshrrev_b32_e32 v3, 4, v4
	v_lshl_add_u32 v2, v3, 7, v2
	v_lshlrev_b32_e32 v2, 2, v2
	v_add_u32_e32 v2, 0x22100, v2
	ds_read_b32 v16, v2
	ds_read_b32 v17, v2 offset:64
	ds_read_b32 v18, v2 offset:128
	ds_read_b32 v19, v2 offset:192
	ds_read_b32 v20, v2 offset:256
	ds_read_b32 v21, v2 offset:320
	ds_read_b32 v22, v2 offset:384
	ds_read_b32 v23, v2 offset:448
	s_waitcnt lgkmcnt(0)
	v_add_f32_e32 v16, v16, v17
	v_add_f32_e32 v16, v16, v18
	v_add_f32_e32 v16, v16, v19
	v_add_f32_e32 v16, v16, v20
	v_add_f32_e32 v16, v16, v21
	v_add_f32_e32 v16, v16, v22
	v_add_f32_e32 v16, v16, v23
	s_barrier
	v_lshlrev_b32_e32 v2, 2, v4
	v_add_u32_e32 v2, 0x22100, v2
	ds_write_b32 v2, v16
	s_waitcnt lgkmcnt(0)
	s_barrier
	v_cmp_gt_u32_e32 vcc, 16, v4
	s_and_saveexec_b64 s[6:7], vcc
	s_cbranch_execz .LBB0_187
	ds_read_b32 v16, v2
	ds_read_b32 v17, v2 offset:64
	ds_read_b32 v18, v2 offset:128
	ds_read_b32 v19, v2 offset:192
	ds_read_b32 v20, v2 offset:256
	ds_read_b32 v21, v2 offset:320
	ds_read_b32 v22, v2 offset:384
	ds_read_b32 v23, v2 offset:448
	ds_read_b32 v24, v2 offset:512
	ds_read_b32 v25, v2 offset:576
	ds_read_b32 v26, v2 offset:640
	ds_read_b32 v27, v2 offset:704
	ds_read_b32 v28, v2 offset:768
	ds_read_b32 v29, v2 offset:832
	ds_read_b32 v30, v2 offset:896
	ds_read_b32 v31, v2 offset:960
	v_lshl_add_u32 v0, s88, 4, v4
	v_lshlrev_b32_e32 v0, 2, v0
	s_add_u32 s8, s4, 0x4300000
	s_addc_u32 s9, s5, 0
	s_waitcnt lgkmcnt(0)
	v_add_f32_e32 v16, v16, v17
	v_add_f32_e32 v16, v16, v18
	v_add_f32_e32 v16, v16, v19
	v_add_f32_e32 v16, v16, v20
	v_add_f32_e32 v16, v16, v21
	v_add_f32_e32 v16, v16, v22
	v_add_f32_e32 v16, v16, v23
	v_add_f32_e32 v16, v16, v24
	v_add_f32_e32 v16, v16, v25
	v_add_f32_e32 v16, v16, v26
	v_add_f32_e32 v16, v16, v27
	v_add_f32_e32 v16, v16, v28
	v_add_f32_e32 v16, v16, v29
	v_add_f32_e32 v16, v16, v30
	v_add_f32_e32 v16, v16, v31
	global_store_dword v0, v16, s[8:9]
